# v23 + XCD stagger of the GEMM-in unit stream, 2.4 us per XCD
# baseline (speedup 1.0000x reference)
.LBB0_151:
	s_and_b32 s89, s78, 7
.Lp1c_stag:
	s_cmp_eq_u32 s89, 0
	s_cbranch_scc1 .Lp1c_stag_done
	s_sleep 90
	s_sub_u32 s89, s89, 1
	s_branch .Lp1c_stag
